# the two units of a workgroup two barriers apart (of three per unit)
# baseline (speedup 1.0000x reference)
.LBB0_427:
	v_or_b32_e32 v3, s3, v7
	v_lshlrev_b32_e32 v3, s1, v3
	v_add_u32_e32 v180, s42, v3
	s_movk_i32 s4, 0x1880
	v_mov_b64_e32 v[10:11], s[84:85]
	v_mad_i64_i32 v[10:11], s[4:5], v180, s4, v[10:11]
	s_lshl_b32 s4, s2, 1
	s_mov_b32 s5, 0
	v_lshl_add_u64 v[10:11], v[10:11], 0, s[4:5]
	v_lshlrev_b32_e32 v12, 4, v6
	v_mov_b32_e32 v13, 0
	v_lshl_add_u64 v[10:11], v[10:11], 0, v[12:13]
	global_load_dwordx4 v[146:149], v[10:11], off offset:96
	global_load_dwordx4 v[150:153], v[10:11], off offset:64
	global_load_dwordx4 v[154:157], v[10:11], off offset:32
	global_load_dwordx4 v[158:161], v[10:11], off
	s_lshl_b32 s81, 1, s1
	s_lshl_b32 s1, 0xffffff80, s1
	s_waitcnt vmcnt(0)
	s_add_i32 s82, s42, s1
	v_lshlrev_b32_e32 v2, 4, v2
	s_movk_i32 s1, 0x1000
	v_add3_u32 v182, v1, v2, s1
	s_movk_i32 s16, 0x1880
	v_and_b32_e32 v100, 63, v0
	v_lshrrev_b32_e32 v101, 3, v100
	v_and_b32_e32 v104, 7, v100
	v_xor_b32_e32 v104, v104, v101
	v_lshlrev_b32_e32 v104, 4, v104
	s_lshl_b32 s10, s88, 7
	s_add_u32 s10, s10, 0x800
	v_add_u32_e32 v104, s10, v104
	s_bfe_u32 s11, s75, 0x2000c
	s_and_b32 s12, s75, 0xffff0000
	s_add_u32 s12, s12, 0x8000
	s_add_u32 s13, s11, 1
	s_lshl_b32 s10, s13, 5
	v_add_u32_e32 v102, s10, v101
	v_mul_u32_u24_e32 v103, s81, v102
	v_add_u32_e32 v103, s82, v103
	s_lshl_b32 s10, s13, 12
	s_add_u32 s10, s10, s12
	s_lshl_b32 s13, s81, 3
	v_max_i32_e32 v106, 0, v103
	s_mov_b32 m0, s10
	v_mad_u32_u24 v108, v106, s16, v104
	global_load_lds_dwordx4 v108, s[84:85]
	v_add_u32_e32 v103, s13, v103
	v_max_i32_e32 v106, 0, v103
	s_add_u32 m0, s10, 0x400
	v_mad_u32_u24 v108, v106, s16, v104
	global_load_lds_dwordx4 v108, s[84:85]
	v_add_u32_e32 v103, s13, v103
	v_max_i32_e32 v106, 0, v103
	s_add_u32 m0, s10, 0x800
	v_mad_u32_u24 v108, v106, s16, v104
	global_load_lds_dwordx4 v108, s[84:85]
	v_add_u32_e32 v103, s13, v103
	v_max_i32_e32 v106, 0, v103
	s_add_u32 m0, s10, 0xc00
	v_mad_u32_u24 v108, v106, s16, v104
	global_load_lds_dwordx4 v108, s[84:85]
	s_add_u32 s13, s11, 4
	s_cmp_eq_u32 s11, 0
	s_cselect_b32 s13, 0, s13
	s_lshl_b32 s10, s13, 5
	v_add_u32_e32 v102, s10, v101
	v_mul_u32_u24_e32 v103, s81, v102
	v_add_u32_e32 v103, s82, v103
	s_lshl_b32 s10, s13, 12
	s_add_u32 s10, s10, s12
	s_lshl_b32 s13, s81, 3
	v_max_i32_e32 v106, 0, v103
	s_mov_b32 m0, s10
	v_mad_u32_u24 v108, v106, s16, v104
	global_load_lds_dwordx4 v108, s[84:85]
	v_add_u32_e32 v103, s13, v103
	v_max_i32_e32 v106, 0, v103
	s_add_u32 m0, s10, 0x400
	v_mad_u32_u24 v108, v106, s16, v104
	global_load_lds_dwordx4 v108, s[84:85]
	v_add_u32_e32 v103, s13, v103
	v_max_i32_e32 v106, 0, v103
	s_add_u32 m0, s10, 0x800
	v_mad_u32_u24 v108, v106, s16, v104
	global_load_lds_dwordx4 v108, s[84:85]
	v_add_u32_e32 v103, s13, v103
	v_max_i32_e32 v106, 0, v103
	s_add_u32 m0, s10, 0xc00
	v_mad_u32_u24 v108, v106, s16, v104
	global_load_lds_dwordx4 v108, s[84:85]
	v_and_b32_e32 v100, 63, v0
	v_lshrrev_b32_e32 v101, 3, v100
	v_and_b32_e32 v104, 7, v100
	v_lshlrev_b32_e32 v104, 4, v104
	s_lshl_b32 s10, s88, 7
	s_add_u32 s10, s10, 0x1000
	v_add_u32_e32 v104, s10, v104
	s_bfe_u32 s11, s75, 0x2000c
	s_and_b32 s12, s75, 0xffff0000
	s_add_u32 s13, s11, 1
	s_lshl_b32 s10, s13, 5
	v_add_u32_e32 v102, s10, v101
	v_mul_u32_u24_e32 v103, s81, v102
	v_add_u32_e32 v103, s82, v103
	s_lshl_b32 s10, s13, 12
	s_add_u32 s10, s10, s12
	s_lshl_b32 s13, s81, 3
	v_max_i32_e32 v106, 0, v103
	s_mov_b32 m0, s10
	v_mad_u32_u24 v108, v106, s16, v104
	global_load_lds_dwordx4 v108, s[84:85]
	v_add_u32_e32 v103, s13, v103
	v_max_i32_e32 v106, 0, v103
	s_add_u32 m0, s10, 0x400
	v_mad_u32_u24 v108, v106, s16, v104
	global_load_lds_dwordx4 v108, s[84:85]
	v_add_u32_e32 v103, s13, v103
	v_max_i32_e32 v106, 0, v103
	s_add_u32 m0, s10, 0x800
	v_mad_u32_u24 v108, v106, s16, v104
	global_load_lds_dwordx4 v108, s[84:85]
	v_add_u32_e32 v103, s13, v103
	v_max_i32_e32 v106, 0, v103
	s_add_u32 m0, s10, 0xc00
	v_mad_u32_u24 v108, v106, s16, v104
	global_load_lds_dwordx4 v108, s[84:85]
	s_add_u32 s13, s11, 4
	s_cmp_eq_u32 s11, 0
	s_cselect_b32 s13, 0, s13
	s_lshl_b32 s10, s13, 5
	v_add_u32_e32 v102, s10, v101
	v_mul_u32_u24_e32 v103, s81, v102
	v_add_u32_e32 v103, s82, v103
	s_lshl_b32 s10, s13, 12
	s_add_u32 s10, s10, s12
	s_lshl_b32 s13, s81, 3
	v_max_i32_e32 v106, 0, v103
	s_mov_b32 m0, s10
	v_mad_u32_u24 v108, v106, s16, v104
	global_load_lds_dwordx4 v108, s[84:85]
	v_add_u32_e32 v103, s13, v103
	v_max_i32_e32 v106, 0, v103
	s_add_u32 m0, s10, 0x400
	v_mad_u32_u24 v108, v106, s16, v104
	global_load_lds_dwordx4 v108, s[84:85]
	v_add_u32_e32 v103, s13, v103
	v_max_i32_e32 v106, 0, v103
	s_add_u32 m0, s10, 0x800
	v_mad_u32_u24 v108, v106, s16, v104
	global_load_lds_dwordx4 v108, s[84:85]
	v_add_u32_e32 v103, s13, v103
	v_max_i32_e32 v106, 0, v103
	s_add_u32 m0, s10, 0xc00
	v_mad_u32_u24 v108, v106, s16, v104
	global_load_lds_dwordx4 v108, s[84:85]
	s_waitcnt vmcnt(0)
	s_barrier
	v_readlane_b32 s10, v254, 14
	s_cmp_eq_u32 s10, 0
	s_cbranch_scc1 .Latt_off0
	s_barrier
	s_barrier

.LBB0_491:
	v_readlane_b32 s0, v254, 14
	s_cmp_eq_u32 s0, 1
	s_cbranch_scc1 .Latt_off1
	s_barrier
	s_barrier
